# speedup vs baseline: 1.0028x; 1.0028x over previous
.LBB0_25:
	v_mfma_f32_32x32x16_f16 v[48:63], v[80:83], v[96:99], 0
	v_add_u32_e32 v209, s8, v226
	ds_read_b128 v[32:35], v209
	ds_read_b128 v[36:39], v209 offset:4352
	ds_read_b128 v[40:43], v209 offset:16
	v_mfma_f32_32x32x16_f16 v[64:79], v[204:207], v[96:99], 0
	s_waitcnt lgkmcnt(2)
	v_mfma_f32_32x32x16_f16 v[48:63], v[88:91], v[32:35], v[48:63]
	ds_read_b128 v[44:47], v209 offset:4368
	v_mfma_f32_32x32x16_f16 v[64:79], v[84:87], v[32:35], v[64:79]
	s_waitcnt lgkmcnt(2)
	v_mfma_f32_32x32x16_f16 v[48:63], v[100:103], v[36:39], v[48:63]
	ds_read_b128 v[32:35], v209 offset:32
	v_mfma_f32_32x32x16_f16 v[64:79], v[92:95], v[36:39], v[64:79]
	s_waitcnt lgkmcnt(2)
	v_mfma_f32_32x32x16_f16 v[48:63], v[108:111], v[40:43], v[48:63]
	ds_read_b128 v[36:39], v209 offset:4384
	v_mfma_f32_32x32x16_f16 v[64:79], v[104:107], v[40:43], v[64:79]
	s_waitcnt lgkmcnt(2)
	v_mfma_f32_32x32x16_f16 v[48:63], v[116:119], v[44:47], v[48:63]
	ds_read_b128 v[40:43], v209 offset:48
	v_mfma_f32_32x32x16_f16 v[64:79], v[112:115], v[44:47], v[64:79]
	s_waitcnt lgkmcnt(2)
	v_mfma_f32_32x32x16_f16 v[48:63], v[120:123], v[32:35], v[48:63]
	ds_read_b128 v[44:47], v209 offset:4400
	v_mfma_f32_32x32x16_f16 v[64:79], v[128:131], v[32:35], v[64:79]
	s_waitcnt lgkmcnt(2)
	v_mfma_f32_32x32x16_f16 v[48:63], v[152:155], v[36:39], v[48:63]
	ds_read_b128 v[32:35], v209 offset:64
	v_mfma_f32_32x32x16_f16 v[64:79], v[124:127], v[36:39], v[64:79]
	s_waitcnt lgkmcnt(2)
	v_mfma_f32_32x32x16_f16 v[48:63], v[136:139], v[40:43], v[48:63]
	ds_read_b128 v[36:39], v209 offset:4416
	v_mfma_f32_32x32x16_f16 v[64:79], v[132:135], v[40:43], v[64:79]
	s_waitcnt lgkmcnt(2)
	v_mfma_f32_32x32x16_f16 v[48:63], v[144:147], v[44:47], v[48:63]
	ds_read_b128 v[40:43], v209 offset:80
	v_mfma_f32_32x32x16_f16 v[64:79], v[140:143], v[44:47], v[64:79]
	s_waitcnt lgkmcnt(2)
	v_mfma_f32_32x32x16_f16 v[48:63], v[156:159], v[32:35], v[48:63]
	ds_read_b128 v[44:47], v209 offset:4432
	v_mfma_f32_32x32x16_f16 v[64:79], v[148:151], v[32:35], v[64:79]
	s_waitcnt lgkmcnt(2)
	v_mfma_f32_32x32x16_f16 v[48:63], v[164:167], v[36:39], v[48:63]
	ds_read_b128 v[32:35], v209 offset:96
	v_mfma_f32_32x32x16_f16 v[64:79], v[160:163], v[36:39], v[64:79]
	s_waitcnt lgkmcnt(2)
	v_mfma_f32_32x32x16_f16 v[48:63], v[172:175], v[40:43], v[48:63]
	ds_read_b128 v[36:39], v209 offset:4448
	v_mfma_f32_32x32x16_f16 v[64:79], v[168:171], v[40:43], v[64:79]
	s_waitcnt lgkmcnt(2)
	v_mfma_f32_32x32x16_f16 v[48:63], v[180:183], v[44:47], v[48:63]
	v_mfma_f32_32x32x16_f16 v[64:79], v[176:179], v[44:47], v[64:79]
	s_waitcnt lgkmcnt(1)
	v_mfma_f32_32x32x16_f16 v[48:63], v[188:191], v[32:35], v[48:63]
	v_mfma_f32_32x32x16_f16 v[64:79], v[184:187], v[32:35], v[64:79]
	s_waitcnt lgkmcnt(0)
	v_mfma_f32_32x32x16_f16 v[48:63], v[196:199], v[36:39], v[48:63]
	v_mfma_f32_32x32x16_f16 v[64:79], v[192:195], v[36:39], v[64:79]
	s_cmp_eq_u32 s3, 3
	s_cbranch_scc0 .Lno_pre
	s_cmpk_eq_i32 s8, 0x600
	s_cbranch_scc0 .Lno_pre
	v_mul_u32_u24_e32 v100, 0x4400, v213
	v_add_u32_e32 v100, v100, v210
	v_mov_b32_e32 v101, 0
	v_readfirstlane_b32 s90, v213
	v_lshl_add_u64 v[100:101], v[100:101], 0, s[36:37]
	s_mul_i32 s90, s90, 0x4540
	s_mov_b32 m0, s90
	s_nop 0
	global_load_lds_dwordx4 v[100:101], off
	global_load_lds_dwordx4 v[100:101], off offset:1024
	global_load_lds_dwordx4 v[100:101], off offset:2048
	global_load_lds_dwordx4 v[100:101], off offset:3072
	s_mov_b64 s[92:93], 0x1000
	v_lshl_add_u64 v[102:103], v[100:101], 0, s[92:93]
	s_add_u32 s91, s90, 0x1000
	s_mov_b32 m0, s91
	s_nop 0
	global_load_lds_dwordx4 v[102:103], off
	global_load_lds_dwordx4 v[102:103], off offset:1024
	global_load_lds_dwordx4 v[102:103], off offset:2048
	global_load_lds_dwordx4 v[102:103], off offset:3072
	s_mov_b64 s[92:93], 0x2000
	v_lshl_add_u64 v[102:103], v[100:101], 0, s[92:93]
	s_add_u32 s91, s90, 0x2000
	s_mov_b32 m0, s91
	s_nop 0
	global_load_lds_dwordx4 v[102:103], off
	s_mov_b64 s[92:93], 0x3800
	v_lshl_add_u64 v[102:103], v[100:101], 0, s[92:93]
	s_add_u32 s91, s90, 0x3800
	s_mov_b32 m0, s91
	s_nop 0
	global_load_lds_dwordx4 v[102:103], off
	global_load_lds_dwordx4 v[102:103], off offset:1024
	global_load_lds_dwordx4 v[102:103], off offset:2048
	s_mov_b64 s[92:93], 0x2400
	v_lshl_add_u64 v[102:103], v[100:101], 0, s[92:93]
	global_load_dwordx4 v[104:107], v[102:103], off
	global_load_dwordx4 v[108:111], v[102:103], off offset:1024
	global_load_dwordx4 v[112:115], v[102:103], off offset:2048
	global_load_dwordx4 v[116:119], v[102:103], off offset:3072
	s_mov_b64 s[92:93], 0x3400
	v_lshl_add_u64 v[102:103], v[100:101], 0, s[92:93]
	global_load_dwordx4 v[120:123], v[102:103], off
